# candidate read-back: 10 strided two-entry reads + 3-VALU mask/adjust per entry instead of 20 exec-masked reads; variant-size bound instead of exact emax (on top of v45)
# speedup vs baseline: 1.0122x; 1.0014x over previous
.LBB0_777:
	s_mov_b64 s[0:1], 0
	s_cbranch_execz .LBB0_921
	s_waitcnt lgkmcnt(0)
	ds_read2st64_b32 v[14:15], v79 offset0:0 offset1:1
	ds_read2st64_b32 v[16:17], v79 offset0:2 offset1:3
	ds_read2st64_b32 v[18:19], v79 offset0:4 offset1:5
	ds_read2st64_b32 v[20:21], v79 offset0:6 offset1:7
	ds_read2st64_b32 v[22:23], v79 offset0:8 offset1:9
	ds_read2st64_b32 v[24:25], v79 offset0:10 offset1:11
	ds_read2st64_b32 v[26:27], v79 offset0:12 offset1:13
	ds_read2st64_b32 v[28:29], v79 offset0:14 offset1:15
	ds_read2st64_b32 v[30:31], v79 offset0:16 offset1:17
	ds_read2st64_b32 v[32:33], v79 offset0:18 offset1:19
	v_cmp_lt_u32_e32 vcc, 12, v91
	v_cmp_lt_u32_e64 s[0:1], 16, v91
	s_cmp_lg_u64 vcc, 0
	s_cselect_b32 s8, 16, 12
	s_cmp_lg_u64 s[0:1], 0
	s_cselect_b32 s8, 20, s8
	s_waitcnt lgkmcnt(9)
	v_cmp_lt_u32_e32 vcc, 0, v91
	v_cmp_lt_u32_e64 s[0:1], 1, v91
	v_sub_u32_e32 v14, v14, v11
	v_sub_u32_e32 v15, v15, v11
	v_cndmask_b32_e32 v90, 0, v14, vcc
	v_cndmask_b32_e64 v88, 0, v15, s[0:1]
	s_waitcnt lgkmcnt(8)
	v_cmp_lt_u32_e32 vcc, 2, v91
	v_cmp_lt_u32_e64 s[0:1], 3, v91
	v_sub_u32_e32 v16, v16, v11
	v_sub_u32_e32 v17, v17, v11
	v_cndmask_b32_e32 v89, 0, v16, vcc
	v_cndmask_b32_e64 v86, 0, v17, s[0:1]
	s_waitcnt lgkmcnt(7)
	v_cmp_lt_u32_e32 vcc, 4, v91
	v_cmp_lt_u32_e64 s[0:1], 5, v91
	v_sub_u32_e32 v18, v18, v11
	v_sub_u32_e32 v19, v19, v11
	v_cndmask_b32_e32 v87, 0, v18, vcc
	v_cndmask_b32_e64 v84, 0, v19, s[0:1]
	s_waitcnt lgkmcnt(6)
	v_cmp_lt_u32_e32 vcc, 6, v91
	v_cmp_lt_u32_e64 s[0:1], 7, v91
	v_sub_u32_e32 v20, v20, v11
	v_sub_u32_e32 v21, v21, v11
	v_cndmask_b32_e32 v85, 0, v20, vcc
	v_cndmask_b32_e64 v82, 0, v21, s[0:1]
	s_waitcnt lgkmcnt(5)
	v_cmp_lt_u32_e32 vcc, 8, v91
	v_cmp_lt_u32_e64 s[0:1], 9, v91
	v_sub_u32_e32 v22, v22, v11
	v_sub_u32_e32 v23, v23, v11
	v_cndmask_b32_e32 v83, 0, v22, vcc
	v_cndmask_b32_e64 v80, 0, v23, s[0:1]
	s_waitcnt lgkmcnt(4)
	v_cmp_lt_u32_e32 vcc, 10, v91
	v_cmp_lt_u32_e64 s[0:1], 11, v91
	v_sub_u32_e32 v24, v24, v11
	v_sub_u32_e32 v25, v25, v11
	v_cndmask_b32_e32 v81, 0, v24, vcc
	v_cndmask_b32_e64 v9, 0, v25, s[0:1]
	s_waitcnt lgkmcnt(3)
	v_cmp_lt_u32_e32 vcc, 12, v91
	v_cmp_lt_u32_e64 s[0:1], 13, v91
	v_sub_u32_e32 v26, v26, v11
	v_sub_u32_e32 v27, v27, v11
	v_cndmask_b32_e32 v78, 0, v26, vcc
	v_cndmask_b32_e64 v7, 0, v27, s[0:1]
	s_waitcnt lgkmcnt(2)
	v_cmp_lt_u32_e32 vcc, 14, v91
	v_cmp_lt_u32_e64 s[0:1], 15, v91
	v_sub_u32_e32 v28, v28, v11
	v_sub_u32_e32 v29, v29, v11
	v_cndmask_b32_e32 v8, 0, v28, vcc
	v_cndmask_b32_e64 v5, 0, v29, s[0:1]
	s_waitcnt lgkmcnt(1)
	v_cmp_lt_u32_e32 vcc, 16, v91
	v_cmp_lt_u32_e64 s[0:1], 17, v91
	v_sub_u32_e32 v30, v30, v11
	v_sub_u32_e32 v31, v31, v11
	v_cndmask_b32_e32 v6, 0, v30, vcc
	v_cndmask_b32_e64 v3, 0, v31, s[0:1]
	s_waitcnt lgkmcnt(0)
	v_cmp_lt_u32_e32 vcc, 18, v91
	v_cmp_lt_u32_e64 s[0:1], 19, v91
	v_sub_u32_e32 v32, v32, v11
	v_sub_u32_e32 v33, v33, v11
	v_cndmask_b32_e32 v4, 0, v32, vcc
	v_cndmask_b32_e64 v2, 0, v33, s[0:1]
	s_lshl_b32 s10, s94, 23
	s_cmp_gt_u32 s8, 12
	s_mov_b64 s[0:1], -1
	s_cbranch_scc0 .LBB0_873
	s_cmp_lt_u32 s8, 17
	s_cbranch_scc1 .LBB0_826
	s_mov_b32 s0, 23
	s_mov_b32 s9, s10
